# speedup vs baseline: 1.0678x; 1.0202x over previous
.LBB2_57:
	v_readlane_b32 s44, v252, 28
	v_readlane_b32 s45, v252, 29
	s_andn2_b64 vcc, exec, s[44:45]
	v_readlane_b32 s48, v252, 33
	v_readlane_b32 s49, v252, 34
	v_readlane_b32 s50, v252, 35
	s_waitcnt lgkmcnt(0)
	s_barrier
	s_cbranch_vccnz .LBB2_1
	ds_read2st64_b32 v[4:5], v207 offset0:128 offset1:132
	v_max_f32_e32 v2, v232, v232
	ds_read2st64_b32 v[44:45], v207 offset0:64 offset1:68
	s_waitcnt lgkmcnt(1)
	v_max_f32_e32 v38, v4, v4
	v_max_f32_e32 v2, v2, v38
	v_sub_f32_e32 v38, v232, v2
	v_sub_f32_e32 v2, v4, v2
	v_exp_f32_e32 v39, v2
	v_exp_f32_e32 v38, v38
	v_mov_b32_e32 v165, v5
	v_mul_f32_e32 v2, v5, v39
	v_pk_fma_f32 v[4:5], v[164:165], v[38:39], v[2:3] op_sel_hi:[1,1,0]
	s_nop 0
	v_mov_b32_e32 v2, v4
	s_nop 1
	v_permlane32_swap_b32_e32 v4, v2
	v_add_f32_e32 v2, v4, v2
	v_div_scale_f32 v4, s[0:1], v2, v2, 1.0
	v_rcp_f32_e32 v5, v4
	v_div_scale_f32 v40, vcc, 1.0, v2, 1.0
	v_readlane_b32 s0, v252, 37
	v_fma_f32 v41, -v4, v5, 1.0
	v_fmac_f32_e32 v5, v41, v5
	v_mul_f32_e32 v41, v40, v5
	v_fma_f32 v42, -v4, v41, v40
	v_fmac_f32_e32 v41, v42, v5
	v_fma_f32 v4, -v4, v41, v40
	v_div_fmas_f32 v4, v4, v5, v41
	v_div_fixup_f32 v2, v4, v2, 1.0
	v_mul_f32_e32 v4, v38, v2
	v_mul_f32_e32 v38, v39, v2
	v_or_b32_e32 v2, s0, v0
	v_lshlrev_b64 v[42:43], 11, v[2:3]
	v_lshl_add_u64 v[42:43], v[162:163], 0, v[42:43]
	v_lshlrev_b32_e32 v2, 1, v159
	v_lshl_add_u64 v[42:43], v[42:43], 0, v[2:3]
	ds_read2st64_b32 v[86:87], v207 offset1:4
	ds_read2st64_b32 v[88:89], v207 offset0:8 offset1:12
	ds_read2st64_b32 v[90:91], v207 offset0:16 offset1:20
	ds_read2st64_b32 v[92:93], v207 offset0:24 offset1:28
	ds_read2st64_b32 v[94:95], v207 offset0:32 offset1:36
	ds_read2st64_b32 v[96:97], v207 offset0:40 offset1:44
	ds_read2st64_b32 v[98:99], v207 offset0:48 offset1:52
	ds_read2st64_b32 v[100:101], v207 offset0:56 offset1:60
	s_waitcnt lgkmcnt(7)
	v_pk_mul_f32 v[86:87], v[38:39], v[86:87] op_sel_hi:[0,1]
	v_pk_fma_f32 v[22:23], v[4:5], v[22:23], v[86:87] op_sel_hi:[0,1,1]
	s_waitcnt lgkmcnt(6)
	v_pk_mul_f32 v[88:89], v[38:39], v[88:89] op_sel_hi:[0,1]
	v_pk_fma_f32 v[24:25], v[4:5], v[24:25], v[88:89] op_sel_hi:[0,1,1]
	s_waitcnt lgkmcnt(5)
	v_pk_mul_f32 v[90:91], v[38:39], v[90:91] op_sel_hi:[0,1]
	v_pk_fma_f32 v[26:27], v[4:5], v[26:27], v[90:91] op_sel_hi:[0,1,1]
	s_waitcnt lgkmcnt(4)
	v_pk_mul_f32 v[92:93], v[38:39], v[92:93] op_sel_hi:[0,1]
	v_pk_fma_f32 v[28:29], v[4:5], v[28:29], v[92:93] op_sel_hi:[0,1,1]
	s_waitcnt lgkmcnt(3)
	v_pk_mul_f32 v[94:95], v[38:39], v[94:95] op_sel_hi:[0,1]
	v_pk_fma_f32 v[30:31], v[4:5], v[30:31], v[94:95] op_sel_hi:[0,1,1]
	s_waitcnt lgkmcnt(2)
	v_pk_mul_f32 v[96:97], v[38:39], v[96:97] op_sel_hi:[0,1]
	v_pk_fma_f32 v[32:33], v[4:5], v[32:33], v[96:97] op_sel_hi:[0,1,1]
	s_waitcnt lgkmcnt(1)
	v_pk_mul_f32 v[98:99], v[38:39], v[98:99] op_sel_hi:[0,1]
	v_pk_fma_f32 v[34:35], v[4:5], v[34:35], v[98:99] op_sel_hi:[0,1,1]
	s_waitcnt lgkmcnt(0)
	v_pk_mul_f32 v[100:101], v[38:39], v[100:101] op_sel_hi:[0,1]
	v_pk_fma_f32 v[36:37], v[4:5], v[36:37], v[100:101] op_sel_hi:[0,1,1]
	ds_read2st64_b32 v[102:103], v207 offset0:64 offset1:68
	ds_read2st64_b32 v[104:105], v207 offset0:72 offset1:76
	ds_read2st64_b32 v[106:107], v207 offset0:80 offset1:84
	ds_read2st64_b32 v[108:109], v207 offset0:88 offset1:92
	ds_read2st64_b32 v[110:111], v207 offset0:96 offset1:100
	ds_read2st64_b32 v[112:113], v207 offset0:104 offset1:108
	ds_read2st64_b32 v[114:115], v207 offset0:112 offset1:116
	ds_read2st64_b32 v[116:117], v207 offset0:120 offset1:124
	s_waitcnt lgkmcnt(7)
	v_pk_mul_f32 v[102:103], v[38:39], v[102:103] op_sel_hi:[0,1]
	v_pk_fma_f32 v[6:7], v[4:5], v[6:7], v[102:103] op_sel_hi:[0,1,1]
	s_waitcnt lgkmcnt(6)
	v_pk_mul_f32 v[104:105], v[38:39], v[104:105] op_sel_hi:[0,1]
	v_pk_fma_f32 v[8:9], v[4:5], v[8:9], v[104:105] op_sel_hi:[0,1,1]
	s_waitcnt lgkmcnt(5)
	v_pk_mul_f32 v[106:107], v[38:39], v[106:107] op_sel_hi:[0,1]
	v_pk_fma_f32 v[10:11], v[4:5], v[10:11], v[106:107] op_sel_hi:[0,1,1]
	s_waitcnt lgkmcnt(4)
	v_pk_mul_f32 v[108:109], v[38:39], v[108:109] op_sel_hi:[0,1]
	v_pk_fma_f32 v[12:13], v[4:5], v[12:13], v[108:109] op_sel_hi:[0,1,1]
	s_waitcnt lgkmcnt(3)
	v_pk_mul_f32 v[110:111], v[38:39], v[110:111] op_sel_hi:[0,1]
	v_pk_fma_f32 v[14:15], v[4:5], v[14:15], v[110:111] op_sel_hi:[0,1,1]
	s_waitcnt lgkmcnt(2)
	v_pk_mul_f32 v[112:113], v[38:39], v[112:113] op_sel_hi:[0,1]
	v_pk_fma_f32 v[16:17], v[4:5], v[16:17], v[112:113] op_sel_hi:[0,1,1]
	s_waitcnt lgkmcnt(1)
	v_pk_mul_f32 v[114:115], v[38:39], v[114:115] op_sel_hi:[0,1]
	v_pk_fma_f32 v[18:19], v[4:5], v[18:19], v[114:115] op_sel_hi:[0,1,1]
	s_waitcnt lgkmcnt(0)
	v_pk_mul_f32 v[116:117], v[38:39], v[116:117] op_sel_hi:[0,1]
	v_pk_fma_f32 v[20:21], v[4:5], v[20:21], v[116:117] op_sel_hi:[0,1,1]
	v_cvt_pk_f16_f32 v22, v22, v23
	v_cvt_pk_f16_f32 v23, v24, v25
	v_cvt_pk_f16_f32 v24, v26, v27
	v_cvt_pk_f16_f32 v25, v28, v29
	v_cvt_pk_f16_f32 v30, v30, v31
	v_cvt_pk_f16_f32 v31, v32, v33
	v_cvt_pk_f16_f32 v32, v34, v35
	v_cvt_pk_f16_f32 v33, v36, v37
	v_cvt_pk_f16_f32 v6, v6, v7
	v_cvt_pk_f16_f32 v7, v8, v9
	v_cvt_pk_f16_f32 v8, v10, v11
	v_cvt_pk_f16_f32 v9, v12, v13
	v_cvt_pk_f16_f32 v14, v14, v15
	v_cvt_pk_f16_f32 v15, v16, v17
	v_cvt_pk_f16_f32 v16, v18, v19
	v_cvt_pk_f16_f32 v17, v20, v21
	s_nop 1
	v_permlane32_swap_b32_e32 v22, v24
	v_permlane32_swap_b32_e32 v23, v25
	v_permlane32_swap_b32_e32 v30, v32
	v_permlane32_swap_b32_e32 v31, v33
	v_permlane32_swap_b32_e32 v6, v8
	v_permlane32_swap_b32_e32 v7, v9
	v_permlane32_swap_b32_e32 v14, v16
	v_permlane32_swap_b32_e32 v15, v17
	global_store_dwordx4 v[42:43], v[22:25], off
	global_store_dwordx4 v[42:43], v[30:33], off offset:32
	global_store_dwordx4 v[42:43], v[6:9], off offset:64
	global_store_dwordx4 v[42:43], v[14:17], off offset:96
	s_branch .LBB2_1
